# baseline (speedup 1.0000x reference)
.LBB2_10:
	s_or_b64 exec, exec, s[4:5]
	v_and_b32_e32 v66, 15, v0
	v_lshl_or_b32 v66, v76, 6, v66
	v_lshl_add_u32 v67, v77, 8, 0
	v_mul_u32_u24_e32 v66, 0x210, v66
	v_add3_u32 v1, v67, v1, v66
	s_lshl_b64 s[4:5], s[10:11], 2
	s_waitcnt vmcnt(0)
	s_barrier
	ds_write_b128 v1, v[2:5]
	ds_write_b128 v1, v[6:9] offset:64
	ds_write_b128 v1, v[10:13] offset:128
	ds_write_b128 v1, v[14:17] offset:192
	ds_write_b128 v1, v[18:21] offset:8448
	ds_write_b128 v1, v[22:25] offset:8512
	ds_write_b128 v1, v[26:29] offset:8576
	ds_write_b128 v1, v[30:33] offset:8640
	ds_write_b128 v1, v[34:37] offset:16896
	ds_write_b128 v1, v[38:41] offset:16960
	ds_write_b128 v1, v[42:45] offset:17024
	ds_write_b128 v1, v[46:49] offset:17088
	ds_write_b128 v1, v[50:53] offset:25344
	ds_write_b128 v1, v[54:57] offset:25408
	ds_write_b128 v1, v[58:61] offset:25472
	ds_write_b128 v1, v[62:65] offset:25536
	v_and_b32_e32 v1, 31, v0
	s_add_u32 s0, s0, s4
	s_addc_u32 s1, s1, s5
	v_lshlrev_b32_e32 v8, 4, v1
	s_waitcnt lgkmcnt(0)
	s_barrier
	v_mov_b32_e32 v2, v180
	v_mov_b32_e32 v3, v181
	v_mov_b32_e32 v4, v182
	v_mov_b32_e32 v5, v183
	v_lshrrev_b32_e32 v1, 5, v0
	v_or_b32_e32 v7, 0x200, v0
	v_or_b32_e32 v10, 0x600, v0
	v_or_b32_e32 v6, s8, v1
	v_lshrrev_b32_e32 v11, 5, v7
	s_movk_i32 s0, 0x210
	v_lshrrev_b32_e32 v12, 5, v10
	v_add_u32_e32 v50, 0, v8
	v_ashrrev_i32_e32 v7, 31, v6
	v_or_b32_e32 v10, s8, v11
	v_or_b32_e32 v18, 32, v6
	v_or_b32_e32 v20, s8, v12
	v_mad_u32_u24 v1, v1, s0, v50
	v_lshlrev_b64 v[42:43], 13, v[6:7]
	v_mad_u32_u24 v7, v11, s0, v50
	v_ashrrev_i32_e32 v11, 31, v10
	v_ashrrev_i32_e32 v19, 31, v18
	v_mad_u32_u24 v34, v12, s0, v50
	v_ashrrev_i32_e32 v21, 31, v20
	v_lshlrev_b64 v[44:45], 13, v[10:11]
	ds_read_b128 v[10:13], v1
	ds_read_b128 v[14:17], v1 offset:16896
	v_add_u32_e32 v38, 0x8400, v1
	s_add_u32 s2, s2, s4
	v_add_u32_e32 v51, 0x4200, v1
	v_lshlrev_b64 v[46:47], 13, v[18:19]
	v_lshlrev_b64 v[48:49], 13, v[20:21]
	ds_read_b128 v[18:21], v1 offset:33792
	ds_read_b128 v[22:25], v1 offset:50688
	ds_read_b128 v[26:29], v7
	ds_read_b128 v[30:33], v51 offset:50688
	ds_read_b128 v[34:37], v34
	ds_read_b128 v[38:41], v38 offset:50688
	v_mov_b32_e32 v9, 0
	s_addc_u32 s3, s3, s5
	v_lshl_add_u64 v[8:9], s[2:3], 0, v[8:9]
	v_lshl_add_u64 v[42:43], v[8:9], 0, v[42:43]
	v_lshl_add_u64 v[44:45], v[8:9], 0, v[44:45]
	v_lshl_add_u64 v[46:47], v[8:9], 0, v[46:47]
	v_lshl_add_u64 v[48:49], v[8:9], 0, v[48:49]
	v_or_b32_e32 v7, 0xa00, v0
	v_lshrrev_b32_e32 v7, 5, v7
	v_add_u32_e32 v1, 0xc600, v1
	s_waitcnt vmcnt(0) lgkmcnt(7)
	v_pk_add_f32 v[12:13], v[4:5], v[12:13]
	v_pk_add_f32 v[10:11], v[2:3], v[10:11]
	s_waitcnt lgkmcnt(3)
	v_pk_add_f32 v[28:29], v[4:5], v[28:29]
	v_pk_add_f32 v[26:27], v[2:3], v[26:27]
	v_pk_add_f32 v[16:17], v[4:5], v[16:17]
	v_pk_add_f32 v[14:15], v[2:3], v[14:15]
	s_waitcnt lgkmcnt(1)
	v_pk_add_f32 v[36:37], v[4:5], v[36:37]
	v_pk_add_f32 v[34:35], v[2:3], v[34:35]
	global_store_dwordx4 v[42:43], v[10:13], off sc0 sc1 nt
	global_store_dwordx4 v[44:45], v[26:29], off sc0 sc1 nt
	global_store_dwordx4 v[46:47], v[14:17], off sc0 sc1 nt
	global_store_dwordx4 v[48:49], v[34:37], off sc0 sc1 nt
	v_or_b32_e32 v10, 64, v6
	v_ashrrev_i32_e32 v11, 31, v10
	v_lshlrev_b64 v[14:15], 13, v[10:11]
	v_mad_u32_u24 v10, v7, s0, v50
	ds_read_b128 v[10:13], v10
	v_pk_add_f32 v[20:21], v[4:5], v[20:21]
	v_pk_add_f32 v[18:19], v[2:3], v[18:19]
	v_lshl_add_u64 v[14:15], v[8:9], 0, v[14:15]
	global_store_dwordx4 v[14:15], v[18:21], off sc0 sc1 nt
	ds_read_b128 v[14:17], v1 offset:50688
	s_waitcnt lgkmcnt(1)
	v_pk_add_f32 v[12:13], v[4:5], v[12:13]
	v_or_b32_e32 v18, s8, v7
	v_ashrrev_i32_e32 v19, 31, v18
	v_lshlrev_b64 v[18:19], 13, v[18:19]
	v_pk_add_f32 v[10:11], v[2:3], v[10:11]
	v_lshl_add_u64 v[18:19], v[8:9], 0, v[18:19]
	v_or_b32_e32 v1, 0xe00, v0
	global_store_dwordx4 v[18:19], v[10:13], off sc0 sc1 nt
	v_or_b32_e32 v18, 0x60, v6
	v_lshrrev_b32_e32 v1, 5, v1
	v_ashrrev_i32_e32 v19, 31, v18
	v_mad_u32_u24 v7, v1, s0, v50
	v_pk_add_f32 v[10:11], v[2:3], v[22:23]
	v_lshlrev_b64 v[22:23], 13, v[18:19]
	ds_read_b128 v[18:21], v7
	v_pk_add_f32 v[12:13], v[4:5], v[24:25]
	v_lshl_add_u64 v[22:23], v[8:9], 0, v[22:23]
	global_store_dwordx4 v[22:23], v[10:13], off sc0 sc1 nt
	v_or_b32_e32 v22, s8, v1
	v_ashrrev_i32_e32 v23, 31, v22
	v_lshlrev_b64 v[22:23], 13, v[22:23]
	s_waitcnt lgkmcnt(0)
	v_pk_add_f32 v[20:21], v[4:5], v[20:21]
	v_pk_add_f32 v[18:19], v[2:3], v[18:19]
	v_lshl_add_u64 v[22:23], v[8:9], 0, v[22:23]
	global_store_dwordx4 v[22:23], v[18:21], off sc0 sc1 nt
	v_or_b32_e32 v22, 0x80, v6
	v_ashrrev_i32_e32 v23, 31, v22
	v_or_b32_e32 v1, 0x1200, v0
	v_add_u32_e32 v7, 0xc600, v51
	v_lshlrev_b64 v[22:23], 13, v[22:23]
	v_lshrrev_b32_e32 v1, 5, v1
	ds_read_b128 v[10:13], v7 offset:50688
	v_pk_add_f32 v[20:21], v[4:5], v[32:33]
	v_pk_add_f32 v[18:19], v[2:3], v[30:31]
	v_lshl_add_u64 v[22:23], v[8:9], 0, v[22:23]
	v_mad_u32_u24 v7, v1, s0, v50
	global_store_dwordx4 v[22:23], v[18:21], off sc0 sc1 nt
	ds_read_b128 v[18:21], v7
	v_or_b32_e32 v7, 0x1600, v0
	v_or_b32_e32 v26, s8, v1
	v_lshrrev_b32_e32 v7, 5, v7
	v_ashrrev_i32_e32 v27, 31, v26
	v_mad_u32_u24 v22, v7, s0, v50
	v_lshlrev_b64 v[26:27], 13, v[26:27]
	ds_read_b128 v[22:25], v22
	s_waitcnt lgkmcnt(1)
	v_pk_add_f32 v[20:21], v[4:5], v[20:21]
	v_pk_add_f32 v[18:19], v[2:3], v[18:19]
	v_lshl_add_u64 v[26:27], v[8:9], 0, v[26:27]
	global_store_dwordx4 v[26:27], v[18:21], off sc0 sc1 nt
	v_or_b32_e32 v26, 0xa0, v6
	v_ashrrev_i32_e32 v27, 31, v26
	v_lshlrev_b64 v[26:27], 13, v[26:27]
	v_pk_add_f32 v[20:21], v[4:5], v[40:41]
	v_pk_add_f32 v[18:19], v[2:3], v[38:39]
	v_lshl_add_u64 v[26:27], v[8:9], 0, v[26:27]
	global_store_dwordx4 v[26:27], v[18:21], off sc0 sc1 nt
	v_or_b32_e32 v1, 0x1a00, v0
	v_lshrrev_b32_e32 v1, 5, v1
	s_waitcnt lgkmcnt(0)
	v_pk_add_f32 v[18:19], v[2:3], v[22:23]
	v_or_b32_e32 v22, s8, v7
	v_ashrrev_i32_e32 v23, 31, v22
	v_lshlrev_b64 v[22:23], 13, v[22:23]
	v_pk_add_f32 v[20:21], v[4:5], v[24:25]
	v_lshl_add_u64 v[22:23], v[8:9], 0, v[22:23]
	global_store_dwordx4 v[22:23], v[18:21], off sc0 sc1 nt
	v_pk_add_f32 v[16:17], v[4:5], v[16:17]
	v_pk_add_f32 v[14:15], v[2:3], v[14:15]
	v_or_b32_e32 v18, 0xc0, v6
	v_ashrrev_i32_e32 v19, 31, v18
	v_lshlrev_b64 v[18:19], 13, v[18:19]
	v_lshl_add_u64 v[18:19], v[8:9], 0, v[18:19]
	v_mad_u32_u24 v7, v1, s0, v50
	v_or_b32_e32 v0, 0x1e00, v0
	global_store_dwordx4 v[18:19], v[14:17], off sc0 sc1 nt
	ds_read_b128 v[14:17], v7
	v_lshrrev_b32_e32 v7, 5, v0
	v_mad_u32_u24 v0, v7, s0, v50
	ds_read_b128 v[18:21], v0
	v_or_b32_e32 v0, s8, v1
	v_ashrrev_i32_e32 v1, 31, v0
	v_lshlrev_b64 v[0:1], 13, v[0:1]
	s_waitcnt lgkmcnt(1)
	v_pk_add_f32 v[16:17], v[4:5], v[16:17]
	v_pk_add_f32 v[14:15], v[2:3], v[14:15]
	v_lshl_add_u64 v[0:1], v[8:9], 0, v[0:1]
	global_store_dwordx4 v[0:1], v[14:17], off sc0 sc1 nt
	v_or_b32_e32 v0, 0xe0, v6
	v_ashrrev_i32_e32 v1, 31, v0
	v_lshlrev_b64 v[0:1], 13, v[0:1]
	v_pk_add_f32 v[12:13], v[4:5], v[12:13]
	v_pk_add_f32 v[10:11], v[2:3], v[10:11]
	v_lshl_add_u64 v[0:1], v[8:9], 0, v[0:1]
	global_store_dwordx4 v[0:1], v[10:13], off sc0 sc1 nt
	v_add_u32_e32 v0, s8, v7
	v_ashrrev_i32_e32 v1, 31, v0
	v_lshlrev_b64 v[0:1], 13, v[0:1]
	s_waitcnt lgkmcnt(0)
	v_pk_add_f32 v[4:5], v[4:5], v[20:21]
	v_pk_add_f32 v[2:3], v[2:3], v[18:19]
	v_lshl_add_u64 v[0:1], v[8:9], 0, v[0:1]
	global_store_dwordx4 v[0:1], v[2:5], off sc0 sc1 nt
	s_endpgm
